# adds: GU epilogue requests its 8 per-row weight words together with counted waits (no store drain), SORT tile table by rank counting
# speedup vs baseline: 1.0347x; 1.0097x over previous
; __device__ __forceinline__ void phase_sort(Frame& F0, int l) {
;     ...
;     if (F.vcu == F.G - 1) { unsigned* TL = (unsigned*)(F.ws + WS_TILES); const int ntot = tpre[65];
;         for (int i = F.tid; i < ntot; i += 512) { int e = 0; while (e < 64 && i >= tpre[e + 1]) ++e;
;             TL[i] = ((unsigned)e << 16) | (unsigned)(e < 64 ? (segbase[e] >> 8) + (i - tpre[e]) : (SH0 >> 8) + (i - tpre[64])); }
;         if (F.tid == 0) TL[1536] = (unsigned)ntot; }
.LBB0_1437:
	ds_read_b128 v[8:11], v181 offset:4928
	ds_read_b128 v[12:15], v181 offset:4944
	ds_read_b128 v[16:19], v181 offset:4960
	ds_read_b128 v[20:23], v181 offset:4976
	ds_read_b128 v[24:27], v181 offset:4992
	ds_read_b128 v[28:31], v181 offset:5008
	ds_read_b128 v[32:35], v181 offset:5024
	ds_read_b128 v[36:39], v181 offset:5040
	ds_read_b32 v72, v181 offset:5184
	v_mov_b32_e32 v1, 0
	s_waitcnt lgkmcnt(8)
	v_cmp_ge_i32_e32 vcc, v0, v9
	v_cmp_ge_i32_e64 s[0:1], v0, v10
	v_cmp_ge_i32_e64 s[2:3], v0, v11
	v_addc_co_u32_e32 v1, vcc, 0, v1, vcc
	v_addc_co_u32_e64 v1, s[0:1], 0, v1, s[0:1]
	v_addc_co_u32_e64 v1, s[2:3], 0, v1, s[2:3]
	ds_read_b128 v[40:43], v181 offset:5056
	s_waitcnt lgkmcnt(8)
	v_cmp_ge_i32_e32 vcc, v0, v12
	v_cmp_ge_i32_e64 s[0:1], v0, v13
	v_cmp_ge_i32_e64 s[2:3], v0, v14
	v_addc_co_u32_e32 v1, vcc, 0, v1, vcc
	v_addc_co_u32_e64 v1, s[0:1], 0, v1, s[0:1]
	v_addc_co_u32_e64 v1, s[2:3], 0, v1, s[2:3]
	s_waitcnt lgkmcnt(7)
	v_cmp_ge_i32_e32 vcc, v0, v15
	v_cmp_ge_i32_e64 s[0:1], v0, v16
	v_cmp_ge_i32_e64 s[2:3], v0, v17
	v_addc_co_u32_e32 v1, vcc, 0, v1, vcc
	v_addc_co_u32_e64 v1, s[0:1], 0, v1, s[0:1]
	v_addc_co_u32_e64 v1, s[2:3], 0, v1, s[2:3]
	ds_read_b128 v[44:47], v181 offset:5072
	s_waitcnt lgkmcnt(7)
	v_cmp_ge_i32_e32 vcc, v0, v18
	v_cmp_ge_i32_e64 s[0:1], v0, v19
	v_cmp_ge_i32_e64 s[2:3], v0, v20
	v_addc_co_u32_e32 v1, vcc, 0, v1, vcc
	v_addc_co_u32_e64 v1, s[0:1], 0, v1, s[0:1]
	v_addc_co_u32_e64 v1, s[2:3], 0, v1, s[2:3]
	ds_read_b128 v[48:51], v181 offset:5088
	v_cmp_ge_i32_e32 vcc, v0, v21
	v_cmp_ge_i32_e64 s[0:1], v0, v22
	v_cmp_ge_i32_e64 s[2:3], v0, v23
	v_addc_co_u32_e32 v1, vcc, 0, v1, vcc
	v_addc_co_u32_e64 v1, s[0:1], 0, v1, s[0:1]
	v_addc_co_u32_e64 v1, s[2:3], 0, v1, s[2:3]
	ds_read_b128 v[52:55], v181 offset:5104
	s_waitcnt lgkmcnt(8)
	v_cmp_ge_i32_e32 vcc, v0, v24
	v_cmp_ge_i32_e64 s[0:1], v0, v25
	v_cmp_ge_i32_e64 s[2:3], v0, v26
	v_addc_co_u32_e32 v1, vcc, 0, v1, vcc
	v_addc_co_u32_e64 v1, s[0:1], 0, v1, s[0:1]
	v_addc_co_u32_e64 v1, s[2:3], 0, v1, s[2:3]
	s_waitcnt lgkmcnt(7)
	v_cmp_ge_i32_e32 vcc, v0, v27
	v_cmp_ge_i32_e64 s[0:1], v0, v28
	v_cmp_ge_i32_e64 s[2:3], v0, v29
	v_addc_co_u32_e32 v1, vcc, 0, v1, vcc
	v_addc_co_u32_e64 v1, s[0:1], 0, v1, s[0:1]
	v_addc_co_u32_e64 v1, s[2:3], 0, v1, s[2:3]
	ds_read_b128 v[56:59], v181 offset:5120
	s_waitcnt lgkmcnt(7)
	v_cmp_ge_i32_e32 vcc, v0, v30
	v_cmp_ge_i32_e64 s[0:1], v0, v31
	v_cmp_ge_i32_e64 s[2:3], v0, v32
	v_addc_co_u32_e32 v1, vcc, 0, v1, vcc
	v_addc_co_u32_e64 v1, s[0:1], 0, v1, s[0:1]
	v_addc_co_u32_e64 v1, s[2:3], 0, v1, s[2:3]
	ds_read_b128 v[60:63], v181 offset:5136
	v_cmp_ge_i32_e32 vcc, v0, v33
	v_cmp_ge_i32_e64 s[0:1], v0, v34
	v_cmp_ge_i32_e64 s[2:3], v0, v35
	v_addc_co_u32_e32 v1, vcc, 0, v1, vcc
	v_addc_co_u32_e64 v1, s[0:1], 0, v1, s[0:1]
	v_addc_co_u32_e64 v1, s[2:3], 0, v1, s[2:3]
	ds_read_b128 v[64:67], v181 offset:5152
	s_waitcnt lgkmcnt(8)
	v_cmp_ge_i32_e32 vcc, v0, v36
	v_cmp_ge_i32_e64 s[0:1], v0, v37
	v_cmp_ge_i32_e64 s[2:3], v0, v38
	v_addc_co_u32_e32 v1, vcc, 0, v1, vcc
	v_addc_co_u32_e64 v1, s[0:1], 0, v1, s[0:1]
	v_addc_co_u32_e64 v1, s[2:3], 0, v1, s[2:3]
	s_waitcnt lgkmcnt(6)
	v_cmp_ge_i32_e32 vcc, v0, v39
	v_cmp_ge_i32_e64 s[0:1], v0, v40
	v_cmp_ge_i32_e64 s[2:3], v0, v41
	v_addc_co_u32_e32 v1, vcc, 0, v1, vcc
	v_addc_co_u32_e64 v1, s[0:1], 0, v1, s[0:1]
	v_addc_co_u32_e64 v1, s[2:3], 0, v1, s[2:3]
	ds_read_b128 v[68:71], v181 offset:5168
	s_waitcnt lgkmcnt(6)
	v_cmp_ge_i32_e32 vcc, v0, v42
	v_cmp_ge_i32_e64 s[0:1], v0, v43
	v_cmp_ge_i32_e64 s[2:3], v0, v44
	v_addc_co_u32_e32 v1, vcc, 0, v1, vcc
	v_addc_co_u32_e64 v1, s[0:1], 0, v1, s[0:1]
	v_addc_co_u32_e64 v1, s[2:3], 0, v1, s[2:3]
	v_cmp_ge_i32_e32 vcc, v0, v45
	v_cmp_ge_i32_e64 s[0:1], v0, v46
	v_cmp_ge_i32_e64 s[2:3], v0, v47
	v_addc_co_u32_e32 v1, vcc, 0, v1, vcc
	v_addc_co_u32_e64 v1, s[0:1], 0, v1, s[0:1]
	v_addc_co_u32_e64 v1, s[2:3], 0, v1, s[2:3]
	s_waitcnt lgkmcnt(5)
	v_cmp_ge_i32_e32 vcc, v0, v48
	v_cmp_ge_i32_e64 s[0:1], v0, v49
	v_cmp_ge_i32_e64 s[2:3], v0, v50
	v_addc_co_u32_e32 v1, vcc, 0, v1, vcc
	v_addc_co_u32_e64 v1, s[0:1], 0, v1, s[0:1]
	v_addc_co_u32_e64 v1, s[2:3], 0, v1, s[2:3]
	s_waitcnt lgkmcnt(4)
	v_cmp_ge_i32_e32 vcc, v0, v51
	v_cmp_ge_i32_e64 s[0:1], v0, v52
	v_cmp_ge_i32_e64 s[2:3], v0, v53
	v_addc_co_u32_e32 v1, vcc, 0, v1, vcc
	v_addc_co_u32_e64 v1, s[0:1], 0, v1, s[0:1]
	v_addc_co_u32_e64 v1, s[2:3], 0, v1, s[2:3]
	s_waitcnt lgkmcnt(3)
	v_cmp_ge_i32_e32 vcc, v0, v54
	v_cmp_ge_i32_e64 s[0:1], v0, v55
	v_cmp_ge_i32_e64 s[2:3], v0, v56
	v_addc_co_u32_e32 v1, vcc, 0, v1, vcc
	v_addc_co_u32_e64 v1, s[0:1], 0, v1, s[0:1]
	v_addc_co_u32_e64 v1, s[2:3], 0, v1, s[2:3]
	v_cmp_ge_i32_e32 vcc, v0, v57
	v_cmp_ge_i32_e64 s[0:1], v0, v58
	v_cmp_ge_i32_e64 s[2:3], v0, v59
	v_addc_co_u32_e32 v1, vcc, 0, v1, vcc
	v_addc_co_u32_e64 v1, s[0:1], 0, v1, s[0:1]
	v_addc_co_u32_e64 v1, s[2:3], 0, v1, s[2:3]
	s_waitcnt lgkmcnt(2)
	v_cmp_ge_i32_e32 vcc, v0, v60
	v_cmp_ge_i32_e64 s[0:1], v0, v61
	v_cmp_ge_i32_e64 s[2:3], v0, v62
	v_addc_co_u32_e32 v1, vcc, 0, v1, vcc
	v_addc_co_u32_e64 v1, s[0:1], 0, v1, s[0:1]
	v_addc_co_u32_e64 v1, s[2:3], 0, v1, s[2:3]
	s_waitcnt lgkmcnt(1)
	v_cmp_ge_i32_e32 vcc, v0, v63
	v_cmp_ge_i32_e64 s[0:1], v0, v64
	v_cmp_ge_i32_e64 s[2:3], v0, v65
	v_addc_co_u32_e32 v1, vcc, 0, v1, vcc
	v_addc_co_u32_e64 v1, s[0:1], 0, v1, s[0:1]
	v_addc_co_u32_e64 v1, s[2:3], 0, v1, s[2:3]
	s_waitcnt lgkmcnt(0)
	v_cmp_ge_i32_e32 vcc, v0, v66
	v_cmp_ge_i32_e64 s[0:1], v0, v67
	v_cmp_ge_i32_e64 s[2:3], v0, v68
	v_addc_co_u32_e32 v1, vcc, 0, v1, vcc
	v_addc_co_u32_e64 v1, s[0:1], 0, v1, s[0:1]
	v_addc_co_u32_e64 v1, s[2:3], 0, v1, s[2:3]
	v_cmp_ge_i32_e32 vcc, v0, v69
	v_cmp_ge_i32_e64 s[0:1], v0, v70
	v_cmp_ge_i32_e64 s[2:3], v0, v71
	v_addc_co_u32_e32 v1, vcc, 0, v1, vcc
	v_addc_co_u32_e64 v1, s[0:1], 0, v1, s[0:1]
	v_addc_co_u32_e64 v1, s[2:3], 0, v1, s[2:3]
	v_cmp_ge_i32_e32 vcc, v0, v72
	s_nop 1
	v_addc_co_u32_e32 v1, vcc, 0, v1, vcc
	v_readlane_b32 s70, v254, 46
	v_readlane_b32 s71, v254, 47
.LBB0_1508:
	v_cmp_lt_u32_e32 vcc, 63, v1
	s_and_saveexec_b64 s[0:1], vcc
	s_xor_b64 s[0:1], exec, s[0:1]
	s_cbranch_execz .LBB0_1510
	ds_read_b32 v3, v181 offset:5184
	s_waitcnt lgkmcnt(0)
	v_sub_u32_e32 v3, v0, v3
	v_add_u32_e32 v3, 0x480, v3

; __device__ __forceinline__ unsigned pk4f8(float a, float b, float c, float d) { int w = 0; w = __builtin_amdgcn_cvt_pk_fp8_f32(a, b, w, false); w = __builtin_amdgcn_cvt_pk_fp8_f32(c, d, w, true); return (unsigned)w; }
;     __device__ __forceinline__ void operator()(const f32x4 (&acc)[2][2][4][2], const Unit& u, int wr, int wc, int fr, int fq) const {
;     ...
;                 for (int dm = 0; dm < 2; ++dm) { const int m = mp + dm; const int row = row0 + ai * HALF + m * 16; const float w = swt[row];
;                     float h[8];
; #pragma unroll
;                     for (int n = 0; n < 2; ++n)
; #pragma unroll
;                         for (int j = 0; j < 4; ++j) { const float g = acc[ai][0][m][n][j], up = acc[ai][1][m][n][j];
;                             const float s = g * __builtin_amdgcn_rcpf(1.0f + __builtin_amdgcn_exp2f(-1.4426950408889634f * g)); h[n * 4 + j] = s * up * w; }
;                     pk[dm][0] = pk4f8(h[0], h[1], h[2], h[3]); pk[dm][1] = pk4f8(h[4], h[5], h[6], h[7]); }
;                 { auto r = __builtin_amdgcn_permlane16_swap(pk[0][0], pk[1][0], false, false); pk[0][0] = r[0]; pk[1][0] = r[1]; }
;                 { auto r = __builtin_amdgcn_permlane16_swap(pk[0][1], pk[1][1], false, false); pk[0][1] = r[0]; pk[1][1] = r[1]; }
;                 u32x4 o; o.x = pk[0][0]; o.y = pk[0][1]; o.z = pk[1][0]; o.w = pk[1][1];
;                 const int row = row0 + ai * HALF + (mp + (fq & 1)) * 16;
;                 *(u32x4*)(H + (size_t)row * 256 + col0) = o; }
.LBB0_1608:
	s_lshl_b32 s0, s29, 8
	v_mov_b32_e32 v10, v200
	v_add_u32_e32 v0, s0, v165
	s_lshl_b32 s0, s44, 7
	v_and_or_b32 v8, v10, 15, v0
	v_ashrrev_i32_e32 v0, 1, v10
	v_ashrrev_i32_e32 v9, 31, v8
	s_or_b32 s0, s0, s6
	v_and_b32_e32 v0, -16, v0
	v_lshl_add_u64 v[6:7], v[8:9], 2, s[42:43]
	v_add_u32_e32 v4, s0, v0
	global_load_dword v18, v[6:7], off
	global_load_dword v19, v[6:7], off offset:64
	global_load_dword v20, v[6:7], off offset:128
	global_load_dword v21, v[6:7], off offset:192
	global_load_dword v22, v[6:7], off offset:512
	global_load_dword v23, v[6:7], off offset:576
	global_load_dword v24, v[6:7], off offset:640
	global_load_dword v25, v[6:7], off offset:704
	v_mul_f32_e32 v1, 0xbfb8aa3b, v156
	v_mul_f32_e32 v2, 0xbfb8aa3b, v157
	v_mul_f32_e32 v3, 0xbfb8aa3b, v158
	v_mul_f32_e32 v9, 0xbfb8aa3b, v159
	v_mul_f32_e32 v11, 0xbfb8aa3b, v152
	v_mul_f32_e32 v12, 0xbfb8aa3b, v153
	v_mul_f32_e32 v13, 0xbfb8aa3b, v154
	v_mul_f32_e32 v14, 0xbfb8aa3b, v155
	v_exp_f32_e32 v1, v1
	v_exp_f32_e32 v2, v2
	v_exp_f32_e32 v3, v3
	v_exp_f32_e32 v9, v9
	v_exp_f32_e32 v11, v11
	v_exp_f32_e32 v12, v12
	v_exp_f32_e32 v13, v13
	v_exp_f32_e32 v14, v14
	v_add_f32_e32 v1, 1.0, v1
	v_add_f32_e32 v2, 1.0, v2
	v_add_f32_e32 v3, 1.0, v3
	v_add_f32_e32 v9, 1.0, v9
	v_add_f32_e32 v11, 1.0, v11
	v_add_f32_e32 v12, 1.0, v12
	v_add_f32_e32 v13, 1.0, v13
	v_add_f32_e32 v14, 1.0, v14
	v_rcp_f32_e32 v1, v1
	v_rcp_f32_e32 v2, v2
	v_rcp_f32_e32 v3, v3
	v_rcp_f32_e32 v9, v9
	v_rcp_f32_e32 v11, v11
	v_rcp_f32_e32 v12, v12
	v_rcp_f32_e32 v13, v13
	v_rcp_f32_e32 v14, v14
	v_mul_f32_e32 v1, v156, v1
	v_mul_f32_e32 v2, v157, v2
	v_mul_f32_e32 v3, v158, v3
	v_mul_f32_e32 v9, v159, v9
	v_mul_f32_e32 v11, v152, v11
	v_mul_f32_e32 v12, v153, v12
	v_mul_f32_e32 v13, v154, v13
	v_mul_f32_e32 v14, v155, v14
	v_mul_f32_e32 v1, v1, v148
	v_mul_f32_e32 v2, v2, v149
	v_mul_f32_e32 v3, v3, v150
	v_mul_f32_e32 v9, v9, v151
	v_mul_f32_e32 v11, v11, v144
	v_mul_f32_e32 v12, v12, v145
	v_mul_f32_e32 v13, v13, v146
	v_mul_f32_e32 v14, v14, v147
	v_mul_f32_e32 v15, 0xbfb8aa3b, v134
	v_mul_f32_e32 v16, 0xbfb8aa3b, v135
	v_exp_f32_e32 v15, v15
	v_exp_f32_e32 v16, v16
	v_ashrrev_i32_e32 v5, 31, v4
	v_mul_f32_e32 v17, 0xbfb8aa3b, v71
	v_add_f32_e32 v15, 1.0, v15
	v_add_f32_e32 v16, 1.0, v16
	v_rcp_f32_e32 v15, v15
	v_rcp_f32_e32 v16, v16
	v_exp_f32_e32 v17, v17
	s_mov_b64 s[0:1], -1
	v_mul_f32_e32 v15, v134, v15
	v_mul_f32_e32 v16, v135, v16
	v_mul_f32_e32 v15, v15, v130
	v_mul_f32_e32 v16, v16, v131
	v_add_f32_e32 v17, 1.0, v17
	v_rcp_f32_e32 v17, v17
	s_and_b64 vcc, exec, s[38:39]
	v_mov_b32_e32 v242, v218
	v_mov_b32_e32 v243, v214
	v_mul_f32_e32 v17, v71, v17
	v_mul_f32_e32 v17, v17, v67
	v_mov_b32_e32 v244, v201
	s_waitcnt vmcnt(7)
	v_mul_f32_e32 v1, v1, v18
	v_mul_f32_e32 v2, v2, v18
	v_mul_f32_e32 v3, v3, v18
	v_mul_f32_e32 v9, v9, v18
	v_mul_f32_e32 v11, v11, v18
	v_mul_f32_e32 v12, v12, v18
	v_mul_f32_e32 v13, v13, v18
	v_mul_f32_e32 v14, v14, v18
	v_mov_b32_e32 v0, v181
	v_cvt_pk_fp8_f32 v0, v1, v2
	v_mov_b32_e32 v1, v181
	v_cvt_pk_fp8_f32 v1, v11, v12
	v_cvt_pk_fp8_f32 v0, v3, v9 op_sel:[0,0,1]
	v_mul_f32_e32 v3, 0xbfb8aa3b, v140
	v_mul_f32_e32 v9, 0xbfb8aa3b, v141
	v_cvt_pk_fp8_f32 v1, v13, v14 op_sel:[0,0,1]
	v_mul_f32_e32 v11, 0xbfb8aa3b, v142
	v_mul_f32_e32 v12, 0xbfb8aa3b, v143
	v_mul_f32_e32 v13, 0xbfb8aa3b, v132
	v_mul_f32_e32 v14, 0xbfb8aa3b, v133
	v_exp_f32_e32 v3, v3
	v_exp_f32_e32 v9, v9
	v_exp_f32_e32 v11, v11
	v_exp_f32_e32 v12, v12
	v_exp_f32_e32 v13, v13
	v_exp_f32_e32 v14, v14
	v_add_f32_e32 v3, 1.0, v3
	v_add_f32_e32 v9, 1.0, v9
	v_add_f32_e32 v11, 1.0, v11
	v_add_f32_e32 v12, 1.0, v12
	v_add_f32_e32 v13, 1.0, v13
	v_add_f32_e32 v14, 1.0, v14
	v_rcp_f32_e32 v3, v3
	v_rcp_f32_e32 v9, v9
	v_rcp_f32_e32 v11, v11
	v_rcp_f32_e32 v12, v12
	v_rcp_f32_e32 v13, v13
	v_rcp_f32_e32 v14, v14
	v_mul_f32_e32 v3, v140, v3
	v_mul_f32_e32 v9, v141, v9
	v_mul_f32_e32 v11, v142, v11
	v_mul_f32_e32 v12, v143, v12
	v_mul_f32_e32 v13, v132, v13
	v_mul_f32_e32 v14, v133, v14
	v_mul_f32_e32 v3, v3, v136
	v_mul_f32_e32 v9, v9, v137
	v_mul_f32_e32 v11, v11, v138
	v_mul_f32_e32 v12, v12, v139
	v_mul_f32_e32 v13, v13, v128
	v_mul_f32_e32 v14, v14, v129
	s_waitcnt vmcnt(6)
	v_mul_f32_e32 v3, v3, v19
	v_mul_f32_e32 v9, v9, v19
	v_mul_f32_e32 v11, v11, v19
	v_mul_f32_e32 v12, v12, v19
	v_mul_f32_e32 v13, v13, v19
	v_mul_f32_e32 v14, v14, v19
	v_mul_f32_e32 v15, v15, v19
	v_mul_f32_e32 v16, v16, v19
	v_mov_b32_e32 v2, v181
	v_cvt_pk_fp8_f32 v2, v3, v9
	v_mov_b32_e32 v3, v181
	v_cvt_pk_fp8_f32 v3, v13, v14
	v_and_b32_e32 v9, 16, v10
	v_cvt_pk_fp8_f32 v2, v11, v12 op_sel:[0,0,1]
	v_or_b32_e32 v10, v8, v9
	v_cvt_pk_fp8_f32 v3, v15, v16 op_sel:[0,0,1]
	v_ashrrev_i32_e32 v11, 31, v10
	v_lshlrev_b64 v[10:11], 8, v[10:11]
	v_lshl_add_u64 v[10:11], s[40:41], 0, v[10:11]
	v_permlane16_swap_b32_e32 v0, v2
	v_permlane16_swap_b32_e32 v1, v3
	v_lshl_add_u64 v[10:11], v[10:11], 0, v[4:5]
	global_store_dwordx4 v[10:11], v[0:3], off
	s_nop 1
	v_mul_f32_e32 v10, 0xbfb8aa3b, v127
	v_mul_f32_e32 v1, 0xbfb8aa3b, v124
	v_mul_f32_e32 v2, 0xbfb8aa3b, v125
	v_mul_f32_e32 v3, 0xbfb8aa3b, v126
	v_mul_f32_e32 v11, 0xbfb8aa3b, v120
	v_mul_f32_e32 v12, 0xbfb8aa3b, v121
	v_mul_f32_e32 v13, 0xbfb8aa3b, v122
	v_mul_f32_e32 v14, 0xbfb8aa3b, v123
	v_exp_f32_e32 v1, v1
	v_exp_f32_e32 v2, v2
	v_exp_f32_e32 v3, v3
	v_exp_f32_e32 v10, v10
	v_exp_f32_e32 v11, v11
	v_exp_f32_e32 v12, v12
	v_exp_f32_e32 v13, v13
	v_exp_f32_e32 v14, v14
	v_add_f32_e32 v1, 1.0, v1
	v_add_f32_e32 v2, 1.0, v2
	v_add_f32_e32 v3, 1.0, v3
	v_add_f32_e32 v10, 1.0, v10
	v_add_f32_e32 v11, 1.0, v11
	v_add_f32_e32 v12, 1.0, v12
	v_add_f32_e32 v13, 1.0, v13
	v_add_f32_e32 v14, 1.0, v14
	v_rcp_f32_e32 v1, v1
	v_rcp_f32_e32 v2, v2
	v_rcp_f32_e32 v3, v3
	v_rcp_f32_e32 v10, v10
	v_rcp_f32_e32 v11, v11
	v_rcp_f32_e32 v12, v12
	v_rcp_f32_e32 v13, v13
	v_rcp_f32_e32 v14, v14
	v_mul_f32_e32 v1, v124, v1
	v_mul_f32_e32 v2, v125, v2
	v_mul_f32_e32 v3, v126, v3
	v_mul_f32_e32 v10, v127, v10
	v_mul_f32_e32 v11, v120, v11
	v_mul_f32_e32 v12, v121, v12
	v_mul_f32_e32 v13, v122, v13
	v_mul_f32_e32 v14, v123, v14
	v_mul_f32_e32 v1, v1, v116
	v_mul_f32_e32 v2, v2, v117
	v_mul_f32_e32 v3, v3, v118
	v_mul_f32_e32 v10, v10, v119
	v_mul_f32_e32 v11, v11, v112
	v_mul_f32_e32 v12, v12, v113
	v_mul_f32_e32 v13, v13, v114
	v_mul_f32_e32 v14, v14, v115
	v_mul_f32_e32 v15, 0xbfb8aa3b, v102
	v_mul_f32_e32 v16, 0xbfb8aa3b, v103
	v_exp_f32_e32 v15, v15
	v_exp_f32_e32 v16, v16
	v_add_f32_e32 v15, 1.0, v15
	v_add_f32_e32 v16, 1.0, v16
	v_rcp_f32_e32 v15, v15
	v_rcp_f32_e32 v16, v16
	v_mul_f32_e32 v15, v102, v15
	v_mul_f32_e32 v16, v103, v16
	v_mul_f32_e32 v15, v15, v98
	v_mul_f32_e32 v16, v16, v99
	s_waitcnt vmcnt(6)
; __device__ __forceinline__ unsigned pk4f8(float a, float b, float c, float d) { int w = 0; w = __builtin_amdgcn_cvt_pk_fp8_f32(a, b, w, false); w = __builtin_amdgcn_cvt_pk_fp8_f32(c, d, w, true); return (unsigned)w; }
;     __device__ __forceinline__ void operator()(const f32x4 (&acc)[2][2][4][2], const Unit& u, int wr, int wc, int fr, int fq) const {
;     ...
;                 for (int dm = 0; dm < 2; ++dm) { const int m = mp + dm; const int row = row0 + ai * HALF + m * 16; const float w = swt[row];
;                     float h[8];
; #pragma unroll
;                     for (int n = 0; n < 2; ++n)
; #pragma unroll
;                         for (int j = 0; j < 4; ++j) { const float g = acc[ai][0][m][n][j], up = acc[ai][1][m][n][j];
;                             const float s = g * __builtin_amdgcn_rcpf(1.0f + __builtin_amdgcn_exp2f(-1.4426950408889634f * g)); h[n * 4 + j] = s * up * w; }
;                     pk[dm][0] = pk4f8(h[0], h[1], h[2], h[3]); pk[dm][1] = pk4f8(h[4], h[5], h[6], h[7]); }
;                 { auto r = __builtin_amdgcn_permlane16_swap(pk[0][0], pk[1][0], false, false); pk[0][0] = r[0]; pk[1][0] = r[1]; }
;                 { auto r = __builtin_amdgcn_permlane16_swap(pk[0][1], pk[1][1], false, false); pk[0][1] = r[0]; pk[1][1] = r[1]; }
;                 u32x4 o; o.x = pk[0][0]; o.y = pk[0][1]; o.z = pk[1][0]; o.w = pk[1][1];
;                 const int row = row0 + ai * HALF + (mp + (fq & 1)) * 16;
;                 *(u32x4*)(H + (size_t)row * 256 + col0) = o; }
	v_mul_f32_e32 v1, v1, v20
	v_mul_f32_e32 v2, v2, v20
	v_mul_f32_e32 v3, v3, v20
	v_mul_f32_e32 v10, v10, v20
	v_mul_f32_e32 v11, v11, v20
	v_mul_f32_e32 v12, v12, v20
	v_mul_f32_e32 v13, v13, v20
	v_mul_f32_e32 v14, v14, v20
	v_mov_b32_e32 v0, v181
	v_cvt_pk_fp8_f32 v0, v1, v2
	v_mov_b32_e32 v1, v181
	v_cvt_pk_fp8_f32 v1, v11, v12
	v_cvt_pk_fp8_f32 v0, v3, v10 op_sel:[0,0,1]
	v_mul_f32_e32 v3, 0xbfb8aa3b, v108
	v_mul_f32_e32 v10, 0xbfb8aa3b, v109
	v_cvt_pk_fp8_f32 v1, v13, v14 op_sel:[0,0,1]
	v_mul_f32_e32 v11, 0xbfb8aa3b, v110
	v_mul_f32_e32 v12, 0xbfb8aa3b, v111
	v_mul_f32_e32 v13, 0xbfb8aa3b, v100
	v_mul_f32_e32 v14, 0xbfb8aa3b, v101
	v_exp_f32_e32 v3, v3
	v_exp_f32_e32 v10, v10
	v_exp_f32_e32 v11, v11
	v_exp_f32_e32 v12, v12
	v_exp_f32_e32 v13, v13
	v_exp_f32_e32 v14, v14
	v_add_f32_e32 v3, 1.0, v3
	v_add_f32_e32 v10, 1.0, v10
	v_add_f32_e32 v11, 1.0, v11
	v_add_f32_e32 v12, 1.0, v12
	v_add_f32_e32 v13, 1.0, v13
	v_add_f32_e32 v14, 1.0, v14
	v_rcp_f32_e32 v3, v3
	v_rcp_f32_e32 v10, v10
	v_rcp_f32_e32 v11, v11
	v_rcp_f32_e32 v12, v12
	v_rcp_f32_e32 v13, v13
	v_rcp_f32_e32 v14, v14
	v_mul_f32_e32 v3, v108, v3
	v_mul_f32_e32 v10, v109, v10
	v_mul_f32_e32 v11, v110, v11
	v_mul_f32_e32 v12, v111, v12
	v_mul_f32_e32 v13, v100, v13
	v_mul_f32_e32 v14, v101, v14
	v_mul_f32_e32 v3, v3, v104
	v_mul_f32_e32 v10, v10, v105
	v_mul_f32_e32 v11, v11, v106
	v_mul_f32_e32 v12, v12, v107
	v_mul_f32_e32 v13, v13, v96
	v_mul_f32_e32 v14, v14, v97
	s_waitcnt vmcnt(5)
	v_mul_f32_e32 v3, v3, v21
	v_mul_f32_e32 v10, v10, v21
	v_mul_f32_e32 v11, v11, v21
	v_mul_f32_e32 v12, v12, v21
	v_mul_f32_e32 v13, v13, v21
	v_mul_f32_e32 v14, v14, v21
	v_mul_f32_e32 v15, v15, v21
	v_mul_f32_e32 v16, v16, v21
	v_mov_b32_e32 v2, v181
	v_cvt_pk_fp8_f32 v2, v3, v10
	v_mov_b32_e32 v3, v181
	v_cvt_pk_fp8_f32 v3, v13, v14
	v_or_b32_e32 v10, 32, v9
	v_cvt_pk_fp8_f32 v2, v11, v12 op_sel:[0,0,1]
	v_or_b32_e32 v12, v10, v8
	v_cvt_pk_fp8_f32 v3, v15, v16 op_sel:[0,0,1]
	v_ashrrev_i32_e32 v13, 31, v12
	v_lshlrev_b64 v[12:13], 8, v[12:13]
	v_lshl_add_u64 v[12:13], s[40:41], 0, v[12:13]
	v_permlane16_swap_b32_e32 v0, v2
	v_permlane16_swap_b32_e32 v1, v3
	v_lshl_add_u64 v[12:13], v[12:13], 0, v[4:5]
	global_store_dwordx4 v[12:13], v[0:3], off
	s_nop 1
	v_mul_f32_e32 v11, 0xbfb8aa3b, v95
	v_mul_f32_e32 v1, 0xbfb8aa3b, v92
	v_mul_f32_e32 v2, 0xbfb8aa3b, v93
	v_mul_f32_e32 v3, 0xbfb8aa3b, v94
	v_mul_f32_e32 v12, 0xbfb8aa3b, v88
	v_mul_f32_e32 v13, 0xbfb8aa3b, v89
	v_mul_f32_e32 v14, 0xbfb8aa3b, v90
	v_mul_f32_e32 v15, 0xbfb8aa3b, v91
	v_exp_f32_e32 v1, v1
	v_exp_f32_e32 v2, v2
	v_exp_f32_e32 v3, v3
	v_exp_f32_e32 v11, v11
	v_exp_f32_e32 v12, v12
	v_exp_f32_e32 v13, v13
	v_exp_f32_e32 v14, v14
	v_exp_f32_e32 v15, v15
	v_add_f32_e32 v1, 1.0, v1
	v_add_f32_e32 v2, 1.0, v2
	v_add_f32_e32 v3, 1.0, v3
	v_add_f32_e32 v11, 1.0, v11
	v_add_f32_e32 v12, 1.0, v12
	v_add_f32_e32 v13, 1.0, v13
	v_add_f32_e32 v14, 1.0, v14
	v_add_f32_e32 v15, 1.0, v15
	v_rcp_f32_e32 v1, v1
	v_rcp_f32_e32 v2, v2
	v_rcp_f32_e32 v3, v3
	v_rcp_f32_e32 v11, v11
	v_rcp_f32_e32 v12, v12
	v_rcp_f32_e32 v13, v13
	v_rcp_f32_e32 v14, v14
	v_rcp_f32_e32 v15, v15
	v_mul_f32_e32 v1, v92, v1
	v_mul_f32_e32 v2, v93, v2
	v_mul_f32_e32 v3, v94, v3
	v_mul_f32_e32 v11, v95, v11
	v_mul_f32_e32 v12, v88, v12
	v_mul_f32_e32 v13, v89, v13
	v_mul_f32_e32 v14, v90, v14
	v_mul_f32_e32 v15, v91, v15
	v_mul_f32_e32 v1, v1, v84
	v_mul_f32_e32 v2, v2, v85
	v_mul_f32_e32 v3, v3, v86
	v_mul_f32_e32 v11, v11, v87
	v_mul_f32_e32 v12, v12, v80
	v_mul_f32_e32 v13, v13, v81
	v_mul_f32_e32 v14, v14, v82
	v_mul_f32_e32 v15, v15, v83
	v_mul_f32_e32 v16, 0xbfb8aa3b, v70
	v_exp_f32_e32 v16, v16
	v_add_u32_e32 v8, 0x80, v8
	v_add_f32_e32 v16, 1.0, v16
	v_rcp_f32_e32 v16, v16
	s_waitcnt vmcnt(5)
	v_mul_f32_e32 v1, v1, v22
	v_mul_f32_e32 v2, v2, v22
	v_mul_f32_e32 v3, v3, v22
	v_mul_f32_e32 v11, v11, v22
	v_mul_f32_e32 v12, v12, v22
	v_mul_f32_e32 v13, v13, v22
	v_mul_f32_e32 v14, v14, v22
	v_mul_f32_e32 v15, v15, v22
	v_mov_b32_e32 v0, v181
	v_cvt_pk_fp8_f32 v0, v1, v2
	v_mov_b32_e32 v1, v181
	v_cvt_pk_fp8_f32 v1, v12, v13
	v_cvt_pk_fp8_f32 v0, v3, v11 op_sel:[0,0,1]
	v_mul_f32_e32 v3, 0xbfb8aa3b, v76
	v_mul_f32_e32 v11, 0xbfb8aa3b, v77
	v_cvt_pk_fp8_f32 v1, v14, v15 op_sel:[0,0,1]
	v_mul_f32_e32 v12, 0xbfb8aa3b, v78
	v_mul_f32_e32 v13, 0xbfb8aa3b, v79
	v_mul_f32_e32 v14, 0xbfb8aa3b, v68
	v_mul_f32_e32 v15, 0xbfb8aa3b, v69
	v_exp_f32_e32 v3, v3
	v_exp_f32_e32 v11, v11
	v_exp_f32_e32 v12, v12
	v_exp_f32_e32 v13, v13
	v_exp_f32_e32 v14, v14
	v_exp_f32_e32 v15, v15
	v_add_f32_e32 v3, 1.0, v3
	v_add_f32_e32 v11, 1.0, v11
	v_add_f32_e32 v12, 1.0, v12
	v_add_f32_e32 v13, 1.0, v13
	v_add_f32_e32 v14, 1.0, v14
	v_add_f32_e32 v15, 1.0, v15
	v_rcp_f32_e32 v3, v3
	v_rcp_f32_e32 v11, v11
	v_rcp_f32_e32 v12, v12
	v_rcp_f32_e32 v13, v13
	v_rcp_f32_e32 v14, v14
	v_rcp_f32_e32 v15, v15
	v_mul_f32_e32 v3, v76, v3
	v_mul_f32_e32 v11, v77, v11
	v_mul_f32_e32 v12, v78, v12
	v_mul_f32_e32 v13, v79, v13
	v_mul_f32_e32 v14, v68, v14
	v_mul_f32_e32 v15, v69, v15
	v_mul_f32_e32 v16, v70, v16
	v_mul_f32_e32 v3, v3, v72
	v_mul_f32_e32 v11, v11, v73
	v_mul_f32_e32 v12, v12, v74
	v_mul_f32_e32 v13, v13, v75
	v_mul_f32_e32 v14, v14, v64
	v_mul_f32_e32 v15, v15, v65
	v_mul_f32_e32 v16, v16, v66
	s_waitcnt vmcnt(4)
; __device__ __forceinline__ unsigned pk4f8(float a, float b, float c, float d) { int w = 0; w = __builtin_amdgcn_cvt_pk_fp8_f32(a, b, w, false); w = __builtin_amdgcn_cvt_pk_fp8_f32(c, d, w, true); return (unsigned)w; }
;     __device__ __forceinline__ void operator()(const f32x4 (&acc)[2][2][4][2], const Unit& u, int wr, int wc, int fr, int fq) const {
;     ...
;                 for (int dm = 0; dm < 2; ++dm) { const int m = mp + dm; const int row = row0 + ai * HALF + m * 16; const float w = swt[row];
;                     float h[8];
; #pragma unroll
;                     for (int n = 0; n < 2; ++n)
; #pragma unroll
;                         for (int j = 0; j < 4; ++j) { const float g = acc[ai][0][m][n][j], up = acc[ai][1][m][n][j];
;                             const float s = g * __builtin_amdgcn_rcpf(1.0f + __builtin_amdgcn_exp2f(-1.4426950408889634f * g)); h[n * 4 + j] = s * up * w; }
;                     pk[dm][0] = pk4f8(h[0], h[1], h[2], h[3]); pk[dm][1] = pk4f8(h[4], h[5], h[6], h[7]); }
;                 { auto r = __builtin_amdgcn_permlane16_swap(pk[0][0], pk[1][0], false, false); pk[0][0] = r[0]; pk[1][0] = r[1]; }
;                 { auto r = __builtin_amdgcn_permlane16_swap(pk[0][1], pk[1][1], false, false); pk[0][1] = r[0]; pk[1][1] = r[1]; }
;                 u32x4 o; o.x = pk[0][0]; o.y = pk[0][1]; o.z = pk[1][0]; o.w = pk[1][1];
;                 const int row = row0 + ai * HALF + (mp + (fq & 1)) * 16;
;                 *(u32x4*)(H + (size_t)row * 256 + col0) = o; }
	v_mul_f32_e32 v3, v3, v23
	v_mul_f32_e32 v11, v11, v23
	v_mul_f32_e32 v12, v12, v23
	v_mul_f32_e32 v13, v13, v23
	v_mul_f32_e32 v14, v14, v23
	v_mul_f32_e32 v15, v15, v23
	v_mul_f32_e32 v16, v16, v23
	v_mul_f32_e32 v17, v17, v23
	v_mov_b32_e32 v2, v181
	v_cvt_pk_fp8_f32 v2, v3, v11
	v_mov_b32_e32 v3, v181
	v_cvt_pk_fp8_f32 v3, v14, v15
	v_mul_f32_e32 v11, 0xbfb8aa3b, v56
	v_cvt_pk_fp8_f32 v2, v12, v13 op_sel:[0,0,1]
	v_or_b32_e32 v12, v8, v9
	v_cvt_pk_fp8_f32 v3, v16, v17 op_sel:[0,0,1]
	v_ashrrev_i32_e32 v13, 31, v12
	v_lshlrev_b64 v[12:13], 8, v[12:13]
	v_lshl_add_u64 v[12:13], s[40:41], 0, v[12:13]
	v_permlane16_swap_b32_e32 v0, v2
	v_permlane16_swap_b32_e32 v1, v3
	v_lshl_add_u64 v[12:13], v[12:13], 0, v[4:5]
	global_store_dwordx4 v[12:13], v[0:3], off
	s_nop 1
	v_mul_f32_e32 v9, 0xbfb8aa3b, v63
	v_mul_f32_e32 v1, 0xbfb8aa3b, v60
	v_mul_f32_e32 v2, 0xbfb8aa3b, v61
	v_mul_f32_e32 v3, 0xbfb8aa3b, v62
	v_mul_f32_e32 v12, 0xbfb8aa3b, v57
	v_mul_f32_e32 v13, 0xbfb8aa3b, v58
	v_mul_f32_e32 v14, 0xbfb8aa3b, v59
	v_exp_f32_e32 v1, v1
	v_exp_f32_e32 v2, v2
	v_exp_f32_e32 v3, v3
	v_exp_f32_e32 v9, v9
	v_exp_f32_e32 v11, v11
	v_exp_f32_e32 v12, v12
	v_exp_f32_e32 v13, v13
	v_exp_f32_e32 v14, v14
	v_add_f32_e32 v1, 1.0, v1
	v_add_f32_e32 v2, 1.0, v2
	v_add_f32_e32 v3, 1.0, v3
	v_add_f32_e32 v9, 1.0, v9
	v_add_f32_e32 v11, 1.0, v11
	v_add_f32_e32 v12, 1.0, v12
	v_add_f32_e32 v13, 1.0, v13
	v_add_f32_e32 v14, 1.0, v14
	v_rcp_f32_e32 v1, v1
	v_rcp_f32_e32 v2, v2
	v_rcp_f32_e32 v3, v3
	v_rcp_f32_e32 v9, v9
	v_rcp_f32_e32 v11, v11
	v_rcp_f32_e32 v12, v12
	v_rcp_f32_e32 v13, v13
	v_rcp_f32_e32 v14, v14
	v_mul_f32_e32 v1, v60, v1
	v_mul_f32_e32 v2, v61, v2
	v_mul_f32_e32 v3, v62, v3
	v_mul_f32_e32 v9, v63, v9
	v_mul_f32_e32 v11, v56, v11
	v_mul_f32_e32 v12, v57, v12
	v_mul_f32_e32 v13, v58, v13
	v_mul_f32_e32 v14, v59, v14
	v_mul_f32_e32 v1, v1, v52
	v_mul_f32_e32 v2, v2, v53
	v_mul_f32_e32 v3, v3, v54
	v_mul_f32_e32 v9, v9, v55
	v_mul_f32_e32 v11, v11, v48
	v_mul_f32_e32 v12, v12, v49
	v_mul_f32_e32 v13, v13, v50
	v_mul_f32_e32 v14, v14, v51
	s_waitcnt vmcnt(4)
	v_mul_f32_e32 v1, v1, v24
	v_mul_f32_e32 v2, v2, v24
	v_mul_f32_e32 v3, v3, v24
	v_mul_f32_e32 v9, v9, v24
	v_mul_f32_e32 v11, v11, v24
	v_mul_f32_e32 v12, v12, v24
	v_mul_f32_e32 v13, v13, v24
	v_mul_f32_e32 v14, v14, v24
	v_mov_b32_e32 v0, v181
	v_cvt_pk_fp8_f32 v0, v1, v2
	v_mov_b32_e32 v1, v181
	v_cvt_pk_fp8_f32 v1, v11, v12
	v_cvt_pk_fp8_f32 v0, v3, v9 op_sel:[0,0,1]
	v_mul_f32_e32 v3, 0xbfb8aa3b, v44
	v_mul_f32_e32 v6, 0xbfb8aa3b, v45
	v_cvt_pk_fp8_f32 v1, v13, v14 op_sel:[0,0,1]
	v_mul_f32_e32 v7, 0xbfb8aa3b, v46
	v_mul_f32_e32 v9, 0xbfb8aa3b, v47
	v_mul_f32_e32 v11, 0xbfb8aa3b, v36
	v_mul_f32_e32 v12, 0xbfb8aa3b, v37
	v_mul_f32_e32 v13, 0xbfb8aa3b, v38
	v_mul_f32_e32 v14, 0xbfb8aa3b, v39
	v_exp_f32_e32 v3, v3
	v_exp_f32_e32 v6, v6
	v_exp_f32_e32 v7, v7
	v_exp_f32_e32 v9, v9
	v_exp_f32_e32 v11, v11
	v_exp_f32_e32 v12, v12
	v_exp_f32_e32 v13, v13
	v_exp_f32_e32 v14, v14
	v_add_f32_e32 v3, 1.0, v3
	v_add_f32_e32 v6, 1.0, v6
	v_add_f32_e32 v7, 1.0, v7
	v_add_f32_e32 v9, 1.0, v9
	v_add_f32_e32 v11, 1.0, v11
	v_add_f32_e32 v12, 1.0, v12
	v_add_f32_e32 v13, 1.0, v13
	v_add_f32_e32 v14, 1.0, v14
	v_rcp_f32_e32 v3, v3
	v_rcp_f32_e32 v6, v6
	v_rcp_f32_e32 v7, v7
	v_rcp_f32_e32 v9, v9
	v_rcp_f32_e32 v11, v11
	v_rcp_f32_e32 v12, v12
	v_rcp_f32_e32 v13, v13
	v_rcp_f32_e32 v14, v14
	v_mul_f32_e32 v3, v44, v3
	v_mul_f32_e32 v6, v45, v6
	v_mul_f32_e32 v7, v46, v7
	v_mul_f32_e32 v9, v47, v9
	v_mul_f32_e32 v11, v36, v11
	v_mul_f32_e32 v12, v37, v12
	v_mul_f32_e32 v13, v38, v13
	v_mul_f32_e32 v14, v39, v14
	v_mul_f32_e32 v3, v3, v40
	v_mul_f32_e32 v6, v6, v41
	v_mul_f32_e32 v7, v7, v42
	v_mul_f32_e32 v9, v9, v43
	v_mul_f32_e32 v11, v11, v32
	v_mul_f32_e32 v12, v12, v33
	v_mul_f32_e32 v13, v13, v34
	v_mul_f32_e32 v14, v14, v35
	s_waitcnt vmcnt(3)
	v_mul_f32_e32 v3, v3, v25
	v_mul_f32_e32 v6, v6, v25
	v_mul_f32_e32 v7, v7, v25
	v_mul_f32_e32 v9, v9, v25
	v_mul_f32_e32 v11, v11, v25
	v_mul_f32_e32 v12, v12, v25
	v_mul_f32_e32 v13, v13, v25
	v_mul_f32_e32 v14, v14, v25
	v_mov_b32_e32 v2, v181
	v_cvt_pk_fp8_f32 v2, v3, v6
	v_mov_b32_e32 v3, v181
	v_cvt_pk_fp8_f32 v3, v11, v12
	v_or_b32_e32 v6, v8, v10
	v_cvt_pk_fp8_f32 v2, v7, v9 op_sel:[0,0,1]
	v_ashrrev_i32_e32 v7, 31, v6
	v_cvt_pk_fp8_f32 v3, v13, v14 op_sel:[0,0,1]
	v_lshlrev_b64 v[6:7], 8, v[6:7]
	v_lshl_add_u64 v[6:7], s[40:41], 0, v[6:7]
	v_permlane16_swap_b32_e32 v0, v2
	v_permlane16_swap_b32_e32 v1, v3
	v_lshl_add_u64 v[4:5], v[6:7], 0, v[4:5]
	global_store_dwordx4 v[4:5], v[0:3], off
	s_cbranch_vccnz .LBB0_1597
; #define PG8_BAR __builtin_amdgcn_s_barrier()
; template <class Sched> __device__ __forceinline__ unsigned gather_off(const Sched& S, int ui, int h, int i, int t, int KB) { asm volatile("" : "+v"(t)); int R, C; stage_rc(t * 16 + i * 8192, R, C); return (unsigned)(S.arow(ui, h * HALF + R) * KB + C * 2); }
;     ...
;         if constexpr (GATHER) {
; #pragma unroll
;             for (int h = 0; h < 2; ++h)
; #pragma unroll
;                 for (int i = 0; i < 2; ++i) oc[h][i] = gather_off(S, ui, h, i, tid, KB); }
;         if constexpr (ALIGN_EPI) { if (wr == 1) PG8_BAR; }
	s_nop 0
	v_mov_b32_e32 v0, v190
	v_mov_b32_e32 v13, 0x2000
	v_ashrrev_i32_e32 v2, 31, v0
	v_lshrrev_b32_e32 v2, 26, v2
	v_lshlrev_b32_e32 v1, 4, v0
	v_add_u32_e32 v2, v0, v2
	v_bfe_i32 v0, v0, 27, 1
	v_lshrrev_b32_e32 v0, 22, v0
	v_add_u32_e32 v0, v1, v0
	v_and_b32_e32 v0, 0xfffffc00, v0
	v_sub_u32_e32 v0, v1, v0
	v_lshrrev_b32_e32 v1, 4, v0
	v_bitop3_b32 v0, v1, v0, 32 bitop3:0x6c
	v_ashrrev_i32_e32 v1, 31, v0
	v_lshrrev_b32_e32 v1, 26, v1
	v_ashrrev_i32_e32 v2, 6, v2
	v_add_u32_e32 v1, v0, v1
	v_ashrrev_i32_e32 v4, 6, v1
	v_lshlrev_b32_e32 v3, 5, v2
	v_lshlrev_b32_e32 v2, 2, v4
	v_and_b32_e32 v4, 0xffffffc0, v3
	v_add3_u32 v2, s23, v2, v4
	v_mov_b32_e32 v4, v190
	ds_read_b32 v2, v2
	s_andn2_b64 vcc, exec, s[36:37]
	v_lshl_add_u32 v4, v4, 4, v13
	v_ashrrev_i32_e32 v5, 31, v4
	v_lshrrev_b32_e32 v5, 22, v5
	v_add_u32_e32 v5, v4, v5
	v_ashrrev_i32_e32 v6, 10, v5
	v_mul_i32_i24_e32 v5, 0x400, v6
	v_sub_u32_e32 v4, v4, v5
	v_lshrrev_b32_e32 v5, 4, v4
	v_bitop3_b32 v4, v5, v4, 32 bitop3:0x6c
	v_ashrrev_i32_e32 v5, 31, v4
	v_lshrrev_b32_e32 v5, 26, v5
	v_add_u32_e32 v5, v4, v5
	v_ashrrev_i32_e32 v8, 6, v5
	v_lshlrev_b32_e32 v7, 5, v6
	v_lshlrev_b32_e32 v6, 2, v8
	v_and_b32_e32 v8, 0xffffffc0, v7
	v_add3_u32 v6, s23, v6, v8
	v_mov_b32_e32 v8, v190
	ds_read_b32 v6, v6
	s_nop 0
	v_ashrrev_i32_e32 v10, 31, v8
	v_lshrrev_b32_e32 v10, 26, v10
	v_lshlrev_b32_e32 v9, 4, v8
	v_add_u32_e32 v10, v8, v10
	v_bfe_i32 v8, v8, 27, 1
	v_lshrrev_b32_e32 v8, 22, v8
	v_add_u32_e32 v8, v9, v8
	v_and_b32_e32 v8, 0xfffffc00, v8
	v_sub_u32_e32 v8, v9, v8
	v_lshrrev_b32_e32 v9, 4, v8
	v_bitop3_b32 v8, v9, v8, 32 bitop3:0x6c
	v_ashrrev_i32_e32 v9, 31, v8
	v_lshrrev_b32_e32 v9, 26, v9
	v_ashrrev_i32_e32 v10, 6, v10
	v_add_u32_e32 v9, v8, v9
	v_ashrrev_i32_e32 v12, 6, v9
	v_lshlrev_b32_e32 v11, 5, v10
	v_lshlrev_b32_e32 v10, 2, v12
	v_and_b32_e32 v12, 0xffffffc0, v11
	v_add3_u32 v10, s23, v10, v12
	v_mov_b32_e32 v12, v190
	ds_read_b32 v10, v10 offset:512
	s_nop 0
	v_lshl_add_u32 v12, v12, 4, v13
	v_ashrrev_i32_e32 v13, 31, v12
	v_lshrrev_b32_e32 v13, 22, v13
	v_add_u32_e32 v13, v12, v13
	v_ashrrev_i32_e32 v14, 10, v13
	v_mul_i32_i24_e32 v13, 0x400, v14
	v_sub_u32_e32 v12, v12, v13
	v_lshrrev_b32_e32 v13, 4, v12
	v_bitop3_b32 v12, v13, v12, 32 bitop3:0x6c
	v_ashrrev_i32_e32 v13, 31, v12
	v_lshrrev_b32_e32 v13, 26, v13
	v_add_u32_e32 v13, v12, v13
	v_ashrrev_i32_e32 v16, 6, v13
	v_lshlrev_b32_e32 v15, 5, v14
	v_lshlrev_b32_e32 v14, 2, v16
	v_and_b32_e32 v16, 0xffffffc0, v15
	v_add3_u32 v14, s23, v14, v16
	ds_read_b32 v14, v14 offset:512
	s_cbranch_vccnz .LBB0_1596
	s_barrier
	s_branch .LBB0_1596
